# MoE down full rounds walk the unit list from the back (most recently written activation panels first), on top of the barrier change
# baseline (speedup 1.0000x reference)
; #define PG8_LDA(dst, b, h) do { _Pragma("unroll") for (int m = 0; m < 4; ++m) _Pragma("unroll") for (int k = 0; k < 2; ++k) dst[m][k] = *(const PG8_LAS bf16x8*)(lds + PG8_SA(b, h) + aoff + m * 2048 + k * 1024); } while (0)
; #define PG8_WAIT_V(n) asm volatile("s_waitcnt vmcnt(" #n ")" ::: "memory")
;     __device__ __forceinline__ bool next(int i, Unit& u) const {
;     ...
;         const int L = l0 + i * G + c; if (L >= nunits) return false;
;         pl = L / NT; n = L - pl * NT; }
;         const int p = p0 + pl;
;         const int e = __builtin_amdgcn_readfirstlane(pexp[p]);
;         u.pm = A_REL ? pl : p; u.po = A_REL ? p : pl; u.pn = n; u.pb = e * NT + n; return true;
; template <class Epi, class Sched, bool ALIGN_EPI = false, bool SP2 = false, bool F8 = false, bool I8 = false, bool PF = false>
; __device__ __forceinline__ void gemm_phase(PG8_LAS unsigned char* lds, const Gemm g, const Sched& S, const Epi& E, const int wave_) {
;     ...
;     Unit cur, nxt; int ui = 0;
;     if (!S.next(0, cur)) return;
;     f32x4 acc[2][2][4][2];
; #pragma unroll
;     for (int a = 0; a < 2; ++a)
; #pragma unroll
;         for (int b = 0; b < 2; ++b)
; #pragma unroll
;             for (int m = 0; m < 4; ++m)
; #pragma unroll
;                 for (int n = 0; n < 2; ++n) acc[a][b][m][n] = (f32x4){0.f, 0.f, 0.f, 0.f};
;     bf16x8 At[4][2], B0[2][2], B1[2][2]; bf16x8 At2[PF ? 4 : 1][2];
;     const char* cA = (const char*)g.A + (size_t)cur.pm * tstep; const char* cB = (const char*)g.Bt + (size_t)cur.pb * tstep;
;     S.a_ready(cur);
;     if constexpr (PF) {
;         PG8_STAGE(PG8_SA(0, 0), cA, voffA); PG8_STAGE(PG8_SB(0, 0), cB, voffB); PG8_STAGE(PG8_SA(0, 1), cA + hstep, voffA); PG8_STAGE(PG8_SB(0, 1), cB + hstep, voffB);
;         PG8_STAGE(PG8_SA(1, 0), cA + kstep, voffA); PG8_STAGE(PG8_SB(1, 0), cB + kstep, voffB);
;         if (wr == 1) { PG8_STAGE(PG8_SA(1, 1), cA + hstep + kstep, voffA); PG8_STAGE(PG8_SB(1, 1), cB + hstep + kstep, voffB); }
;         PG8_WAIT_V(8); PG8_BAR;
;         PG8_LDA(At, 0, 0); PG8_LDB(B0, 0, 0); __builtin_amdgcn_s_waitcnt(0xC07F);
;         if (wr == 1) PG8_BAR;
;     } else
;     if constexpr (SP2) {
;         PG8_STAGE(PG8_SB(0, 0), cB, voffB); PG8_STAGE(PG8_SB(0, 1), cB + hstep, voffB); PG8_STAGE(PG8_SA(0, 0), cA, voffA); PG8_STAGE(PG8_SA(0, 1), cA + hstep, voffA);
;         if (wr == 1) PG8_BAR;
;         PG8_WAIT_V(2); PG8_BAR;
.LBB0_1608:
	v_mov_b32_e32 v0, 0x300000
	global_load_dword v0, v0, s[92:93] offset:1088
	s_abs_i32 s2, s13
	v_cvt_f32_u32_e32 v1, s2
	s_sub_i32 s3, 0, s2
	v_mbcnt_lo_u32_b32 v2, -1, 0
	v_mbcnt_hi_u32_b32 v2, -1, v2
	v_rcp_iflag_f32_e32 v1, v1
	v_add_u32_e32 v8, s96, v2
	v_mul_f32_e32 v1, 0x4f7ffffe, v1
	v_cvt_u32_f32_e32 v1, v1
	s_nop 0
	v_readfirstlane_b32 s6, v1
	s_mul_i32 s3, s3, s6
	s_mul_hi_u32 s3, s6, s3
	s_add_i32 s6, s6, s3
	s_waitcnt vmcnt(0)
	v_readfirstlane_b32 s3, v0
	s_lshl_b32 s41, s3, 2
	s_abs_i32 s7, s41
	s_mul_hi_u32 s6, s7, s6
	s_mul_i32 s6, s6, s2
	s_sub_i32 s6, s7, s6
	s_bfe_i32 s3, s3, 0x1001d
	s_sub_i32 s7, s6, s2
	s_cmp_ge_u32 s6, s2
	s_cselect_b32 s6, s7, s6
	s_sub_i32 s7, s6, s2
	s_cmp_ge_u32 s6, s2
	s_cselect_b32 s2, s7, s6
	s_xor_b32 s2, s2, s3
	s_sub_i32 s2, s3, s2
	s_add_i32 s41, s41, s2
	s_cmp_ge_i32 s40, s41
	v_readfirstlane_b32 s2, v8
	s_cbranch_scc1 .LBB0_1628
	s_ashr_i32 s3, s2, 6
	s_ashr_i32 s8, s2, 8
	s_lshl_b32 s42, s3, 10
	s_add_u32 s43, s92, 0x3c00000
	s_addc_u32 s44, s93, 0
	s_sub_i32 s98, s41, s40
	s_add_i32 s98, s98, -1
	s_ashr_i32 s6, s98, 31
	s_lshr_b32 s6, s6, 30
	s_add_i32 s6, s98, s6
	s_ashr_i32 s28, s6, 2
	s_and_b32 s6, s6, -4
	s_ashr_i32 s29, s28, 31
	s_sub_i32 s70, s98, s6
	s_lshl_b64 s[6:7], s[28:29], 2
	s_add_u32 s6, s62, s6
	s_addc_u32 s7, s63, s7
	v_mov_b32_e32 v161, 0
	global_load_dword v0, v161, s[6:7]
	v_lshlrev_b32_e32 v1, 4, v8
	v_bfe_i32 v3, v8, 27, 1
	v_ashrrev_i32_e32 v4, 31, v8
	v_add_u32_e32 v5, 0x2000, v1
	v_lshrrev_b32_e32 v3, 22, v3
	v_lshrrev_b32_e32 v4, 26, v4
	v_ashrrev_i32_e32 v6, 31, v5
	v_add_u32_e32 v3, v1, v3
	v_add_u32_e32 v4, v8, v4
	v_lshrrev_b32_e32 v6, 22, v6
	v_and_b32_e32 v3, 0xfffffc00, v3
	v_ashrrev_i32_e32 v10, 6, v4
	v_add_u32_e32 v4, v5, v6
	v_sub_u32_e32 v1, v1, v3
	v_lshlrev_b32_e32 v6, 5, v10
	v_ashrrev_i32_e32 v9, 10, v4
	v_lshrrev_b32_e32 v4, 4, v1
	v_and_b32_e32 v12, 32, v6
	v_mul_i32_i24_e32 v6, 0x400, v9
	v_lshlrev_b32_e32 v7, 3, v9
	v_bitop3_b32 v1, v4, v1, 32 bitop3:0x6c
	v_sub_u32_e32 v4, v5, v6
	v_and_b32_e32 v5, -16, v7
	v_ashrrev_i32_e32 v6, 31, v1
	v_lshrrev_b32_e32 v7, 4, v4
	v_lshrrev_b32_e32 v6, 26, v6
	v_bitop3_b32 v4, v7, v4, 32 bitop3:0x6c
	v_lshlrev_b32_e32 v3, 3, v10
	v_add_u32_e32 v6, v1, v6
	v_ashrrev_i32_e32 v7, 31, v4
	v_and_b32_e32 v3, -16, v3
	v_ashrrev_i32_e32 v13, 6, v6
	v_and_b32_e32 v6, 0xc0, v6
	v_lshrrev_b32_e32 v7, 26, v7
	s_mov_b32 s6, 0xffffe0
	v_mov_b32_e32 v2, 1
	v_add_u32_e32 v3, v13, v3
	v_and_b32_e32 v14, 3, v13
	v_sub_u32_e32 v1, v1, v6
	v_add_u32_e32 v6, v4, v7
	v_and_or_b32 v7, v3, s6, v14
	v_lshrrev_b32_e32 v15, 2, v3
	v_ashrrev_i16_sdwa v1, v2, sext(v1) dst_sel:DWORD dst_unused:UNUSED_PAD src0_sel:DWORD src1_sel:BYTE_0
	v_ashrrev_i32_e32 v14, 6, v6
	v_and_b32_e32 v17, 4, v15
	v_bfe_i32 v15, v1, 0, 16
	v_add_u32_e32 v1, v14, v5
	v_and_b32_e32 v5, 3, v14
	v_and_or_b32 v5, v1, s6, v5
	v_lshlrev_b32_e32 v16, 1, v3
	s_movk_i32 s12, 0x700
	v_and_b32_e32 v6, 0xc0, v6
	v_and_b32_e32 v16, 24, v16
	v_mul_lo_u32 v3, v3, s12
	v_sub_u32_e32 v4, v4, v6
	v_or3_b32 v6, v7, v17, v16
	v_add_u32_e32 v7, v12, v15
	v_lshrrev_b32_e32 v16, 2, v1
	v_lshlrev_b32_e32 v17, 1, v1
	v_lshlrev_b32_e32 v11, 5, v9
	v_ashrrev_i16_sdwa v2, v2, sext(v4) dst_sel:DWORD dst_unused:UNUSED_PAD src0_sel:DWORD src1_sel:BYTE_0
	v_mul_u32_u24_e32 v4, 0x700, v6
	v_add_lshl_u32 v162, v7, v3, 1
	v_and_b32_e32 v3, 4, v16
	v_and_b32_e32 v6, 24, v17
	v_and_b32_e32 v11, 32, v11
	v_bfe_i32 v16, v2, 0, 16
	v_add_lshl_u32 v160, v4, v7, 1
	v_or3_b32 v2, v5, v3, v6
	v_add_u32_e32 v3, v11, v16
	v_mul_u32_u24_e32 v2, 0x700, v2
	v_add_lshl_u32 v166, v2, v3, 1
	s_mul_i32 s10, s28, 0xe0000
	s_mul_hi_i32 s9, s28, 0xe0000
	v_mul_lo_u32 v1, v1, s12
	v_add_lshl_u32 v164, v3, v1, 1
	v_mov_b32_e32 v167, v161
	v_mov_b32_e32 v163, v161
	v_mov_b32_e32 v165, v161
	s_waitcnt vmcnt(0)
	v_readfirstlane_b32 s6, v0
	s_lshl_b32 s6, s6, 2
	s_add_i32 s6, s6, s70
	s_mul_hi_i32 s7, s6, 0xe0000
	s_mul_i32 s6, s6, 0xe0000
	s_add_u32 s30, s43, s6
	s_addc_u32 s31, s44, s7
	s_add_i32 s29, s42, 0
	s_add_i32 m0, s29, 0x10000
	s_mov_b32 s48, 0
	global_load_lds_dwordx4 v160, s[30:31]
	s_add_i32 m0, s29, 0x12000
	s_add_u32 s6, s30, 0x70000
	global_load_lds_dwordx4 v166, s[30:31]
	s_addc_u32 s7, s31, 0
	s_add_i32 m0, s29, 0x14000
	v_lshl_add_u64 v[6:7], s[30:31], 0, v[160:161]
	global_load_lds_dwordx4 v160, s[6:7]
	s_add_i32 m0, s29, 0x16000
	s_add_u32 s34, s4, s10
	s_addc_u32 s35, s5, s9
	s_add_i32 s45, s29, 0x2000
	global_load_lds_dwordx4 v166, s[6:7]
	s_mov_b32 m0, s29
	s_add_u32 s6, s34, 0x70000
	global_load_lds_dwordx4 v162, s[34:35]
	s_mov_b32 m0, s45
	s_addc_u32 s7, s35, 0
	s_add_i32 s46, s29, 0x4000
	global_load_lds_dwordx4 v164, s[34:35]
	s_mov_b32 m0, s46
	s_add_i32 s47, s29, 0x6000
	global_load_lds_dwordx4 v162, s[6:7]
	s_mov_b32 m0, s47
	s_cmp_eq_u32 s8, 1
	global_load_lds_dwordx4 v164, s[6:7]
	v_lshl_add_u64 v[4:5], s[30:31], 0, v[166:167]
	v_lshl_add_u64 v[0:1], s[34:35], 0, v[162:163]
	s_cselect_b64 s[6:7], -1, 0
	s_cmp_lg_u32 s8, 1
	v_lshl_add_u64 v[2:3], s[34:35], 0, v[164:165]
	s_cbranch_scc1 .LBB0_1611
	s_barrier

;     __device__ __forceinline__ bool next(int i, Unit& u) const {
;     ...
;         const int L = l0 + i * G + c; if (L >= nunits) return false;
;         pl = L / NT; n = L - pl * NT; }
;         const int p = p0 + pl;
;         const int e = __builtin_amdgcn_readfirstlane(pexp[p]);
;         u.pm = A_REL ? pl : p; u.po = A_REL ? p : pl; u.pn = n; u.pb = e * NT + n; return true;
; template <class Epi, class Sched, bool ALIGN_EPI = false, bool SP2 = false, bool F8 = false, bool I8 = false, bool PF = false>
; __device__ __forceinline__ void gemm_phase(PG8_LAS unsigned char* lds, const Gemm g, const Sched& S, const Epi& E, const int wave_) {
;     ...
;         const bool has_next = S.next(ui + 1, nxt);
;         const char* nA = has_next ? (const char*)g.A + (size_t)nxt.pm * tstep : cA; const char* nB = has_next ? (const char*)g.Bt + (size_t)nxt.pb * tstep : cB;
.LBB0_1614:
	s_add_i32 s48, s48, 1
	s_mul_i32 s2, s48, s13
	s_add_i32 s2, s2, s40
	s_cmp_lt_i32 s2, s41
	s_cselect_b64 s[24:25], -1, 0
	s_cmp_ge_i32 s2, s41
	s_cbranch_scc1 .LBB0_1616
	s_sub_i32 s2, s41, s2
	s_add_i32 s2, s2, -1
	s_ashr_i32 s3, s2, 31
	s_lshr_b32 s3, s3, 30
	s_add_i32 s3, s2, s3
	s_ashr_i32 s22, s3, 2
	s_and_b32 s3, s3, -4
	s_ashr_i32 s23, s22, 31
	s_sub_i32 s67, s2, s3
	s_lshl_b64 s[2:3], s[22:23], 2
	s_add_u32 s2, s62, s2
	s_addc_u32 s3, s63, s3
	global_load_dword v0, v161, s[2:3]
	s_waitcnt vmcnt(0)
	v_readfirstlane_b32 s2, v0
	s_lshl_b32 s2, s2, 2
	s_add_i32 s23, s2, s67

; __global__ void __launch_bounds__(NWAVES * 64, 2) fwd(Args args) {
	.amdhsa_kernel _Z3fwd4Args
		.amdhsa_group_segment_fixed_size 0
		.amdhsa_private_segment_fixed_size 0
		.amdhsa_kernarg_size 544
		.amdhsa_user_sgpr_count 2
		.amdhsa_user_sgpr_dispatch_ptr 0
		.amdhsa_user_sgpr_queue_ptr 0
		.amdhsa_user_sgpr_kernarg_segment_ptr 1
		.amdhsa_user_sgpr_dispatch_id 0
		.amdhsa_user_sgpr_kernarg_preload_length 0
		.amdhsa_user_sgpr_kernarg_preload_offset 0
		.amdhsa_user_sgpr_private_segment_size 0
		.amdhsa_uses_dynamic_stack 0
		.amdhsa_enable_private_segment 0
		.amdhsa_system_sgpr_workgroup_id_x 1
		.amdhsa_system_sgpr_workgroup_id_y 0
		.amdhsa_system_sgpr_workgroup_id_z 0
		.amdhsa_system_sgpr_workgroup_info 0
		.amdhsa_system_vgpr_workitem_id 0
		.amdhsa_next_free_vgpr 255
		.amdhsa_next_free_sgpr 100
		.amdhsa_accum_offset 256
		.amdhsa_reserve_vcc 1
		.amdhsa_float_round_mode_32 0
		.amdhsa_float_round_mode_16_64 0
		.amdhsa_float_denorm_mode_32 3
		.amdhsa_float_denorm_mode_16_64 3
		.amdhsa_dx10_clamp 1
		.amdhsa_ieee_mode 1
		.amdhsa_fp16_overflow 0
		.amdhsa_tg_split 0
		.amdhsa_exception_fp_ieee_invalid_op 0
		.amdhsa_exception_fp_denorm_src 0
		.amdhsa_exception_fp_ieee_div_zero 0
		.amdhsa_exception_fp_ieee_overflow 0
		.amdhsa_exception_fp_ieee_underflow 0
		.amdhsa_exception_fp_ieee_inexact 0
		.amdhsa_exception_int_div_zero 0
	.end_amdhsa_kernel

; __global__ void __launch_bounds__(NWAVES * 64, 2) fwd(Args args) {
amdhsa.kernels:
  - .agpr_count:     0
    .args:
      - .offset:         0
        .size:           288
        .value_kind:     by_value
      - .offset:         288
        .size:           4
        .value_kind:     hidden_block_count_x
      - .offset:         292
        .size:           4
        .value_kind:     hidden_block_count_y
      - .offset:         296
        .size:           4
        .value_kind:     hidden_block_count_z
      - .offset:         300
        .size:           2
        .value_kind:     hidden_group_size_x
      - .offset:         302
        .size:           2
        .value_kind:     hidden_group_size_y
      - .offset:         304
        .size:           2
        .value_kind:     hidden_group_size_z
      - .offset:         306
        .size:           2
        .value_kind:     hidden_remainder_x
      - .offset:         308
        .size:           2
        .value_kind:     hidden_remainder_y
      - .offset:         310
        .size:           2
        .value_kind:     hidden_remainder_z
      - .offset:         328
        .size:           8
        .value_kind:     hidden_global_offset_x
      - .offset:         336
        .size:           8
        .value_kind:     hidden_global_offset_y
      - .offset:         344
        .size:           8
        .value_kind:     hidden_global_offset_z
      - .offset:         352
        .size:           2
        .value_kind:     hidden_grid_dims
      - .offset:         408
        .size:           4
        .value_kind:     hidden_dynamic_lds_size
    .group_segment_fixed_size: 0
    .kernarg_segment_align: 8
    .kernarg_segment_size: 544
    .language:       OpenCL C
    .language_version:
      - 2
      - 0
    .max_flat_workgroup_size: 512
    .name:           _Z3fwd4Args
    .private_segment_fixed_size: 0
    .sgpr_count:     106
    .sgpr_spill_count: 63
    .symbol:         _Z3fwd4Args.kd
    .uniform_work_group_size: 1
    .uses_dynamic_stack: false
    .vgpr_count:     255
    .vgpr_spill_count: 0
    .wavefront_size: 64
